# sparse attention: previous query output block (scale, bf16 convert, stores) deferred behind the next query LDS row staging; invw reads issued early
# speedup vs baseline: 1.0012x; 1.0012x over previous
.LBB0_802:
	s_or_b64 exec, exec, s[4:5]
	v_lshlrev_b32_e32 v11, 2, v90
	v_bfe_u32 v14, v90, 2, 2
	v_and_b32_e32 v11, 12, v11
	v_bitop3_b32 v12, v11, v2, v14 bitop3:0x36
	v_lshlrev_b32_e32 v93, 4, v12
	v_add_u32_e32 v12, 2, v2
	v_bitop3_b32 v12, v11, v12, v14 bitop3:0x36
	v_lshlrev_b32_e32 v94, 4, v12
	v_add_u32_e32 v12, 4, v2
	v_bitop3_b32 v12, v11, v12, v14 bitop3:0x36
	v_lshlrev_b32_e32 v95, 4, v12
	v_add_u32_e32 v12, 6, v2
	v_bitop3_b32 v12, v11, v12, v14 bitop3:0x36
	v_lshlrev_b32_e32 v96, 4, v12
	v_add_u32_e32 v12, 8, v2
	v_bitop3_b32 v12, v11, v12, v14 bitop3:0x36
	v_readlane_b32 s4, v252, 60
	v_lshlrev_b32_e32 v97, 4, v12
	v_add_u32_e32 v12, 10, v2
	s_waitcnt lgkmcnt(0)
	s_mov_b32 s6, s4
	v_bitop3_b32 v12, v11, v12, v14 bitop3:0x36
	v_add_lshl_u32 v9, v2, s6, 8
	v_lshlrev_b32_e32 v1, 6, v2
	v_lshlrev_b32_e32 v98, 4, v12
	v_add_u32_e32 v12, 12, v2
	v_add_u32_e32 v2, 14, v2
	v_bitop3_b32 v2, v11, v2, v14 bitop3:0x36
	v_lshlrev_b32_e32 v100, 4, v2
	v_lshrrev_b32_e32 v2, 3, v90
	s_movk_i32 s4, 0xf0
	v_bitop3_b32 v12, v11, v12, v14 bitop3:0x36
	v_and_b32_e32 v15, 0x1ffffffc, v2
	v_bitop3_b32 v92, v1, v4, s4 bitop3:0x78
	v_lshlrev_b32_e32 v99, 4, v12
	v_add_u32_e32 v12, 8, v15
	v_and_b32_e32 v2, 2, v2
	v_bfe_u32 v81, v90, 1, 1
	v_readlane_b32 s4, v253, 16
	v_bfe_u32 v11, v12, 2, 2
	v_lshlrev_b32_e32 v80, 2, v14
	v_or3_b32 v81, v2, s4, v81
	v_bitop3_b32 v2, v11, v81, v80 bitop3:0x36
	v_lshlrev_b32_e32 v11, 4, v2
	v_or_b32_e32 v2, v12, v14
	v_lshlrev_b32_e32 v12, 8, v2
	v_and_b32_e32 v2, 8, v13
	v_bfe_u32 v13, v90, 5, 2
	v_or_b32_e32 v14, v15, v14
	v_ashrrev_i32_e32 v15, 3, v90
	v_readlane_b32 s4, v253, 18
	v_bitop3_b32 v13, v80, v81, v13 bitop3:0x36
	v_readlane_b32 s5, v252, 61
	v_add_u32_e32 v80, s4, v15
	v_lshlrev_b32_e32 v81, 9, v80
	v_readlane_b32 s4, v253, 14
	v_and_b32_e32 v88, 0xfffffc00, v81
	v_lshlrev_b32_e32 v15, 5, v15
	v_and_or_b32 v81, v90, 7, s4
	v_lshl_add_u32 v84, v81, 5, v80
	v_add_u32_e32 v80, 0x100, v84
	v_readlane_b32 s4, v253, 19
	v_and_or_b32 v15, v15, 32, v81
	v_ashrrev_i32_e32 v81, 31, v80
	v_readlane_b32 s5, v253, 20
	v_ashrrev_i32_e32 v85, 31, v84
	v_lshlrev_b32_e32 v0, 12, v90
	v_lshl_add_u64 v[80:81], v[80:81], 4, s[4:5]
	v_lshl_add_u64 v[84:85], v[84:85], 4, s[4:5]
	global_load_dwordx4 v[80:83], v[80:81], off
	s_add_i32 s4, 0, 0x20000
	global_load_dwordx4 v[84:87], v[84:85], off
	v_and_b32_e32 v0, 0x10000, v0
	v_and_or_b32 v10, v90, 31, s6
	v_lshlrev_b32_e32 v13, 4, v13
	v_lshlrev_b32_e32 v14, 8, v14
	v_lshl_add_u32 v15, v15, 4, s4
	v_readlane_b32 s4, v253, 23
	v_xor_b32_e32 v1, 0x80, v92
	v_xor_b32_e32 v3, 16, v92
	v_xor_b32_e32 v4, 0x90, v92
	v_xor_b32_e32 v5, 32, v92
	v_xor_b32_e32 v6, 0xa0, v92
	v_xor_b32_e32 v7, 48, v92
	v_xor_b32_e32 v8, 0xb0, v92
	v_add3_u32 v13, s4, v13, v14
	v_add3_u32 v11, s4, v11, v12
	v_add3_u32 v101, 0, v9, v0
	v_lshl_add_u32 v102, v10, 8, 0
	v_readlane_b32 s4, v255, 10
	v_readlane_b32 s6, v254, 56
	v_add_u32_e32 v103, 0x10000, v102
	s_mov_b32 s14, 0
	v_add_u32_e32 v104, v101, v1
	v_add_u32_e32 v105, v101, v3
	v_add_u32_e32 v106, v101, v4
	v_add_u32_e32 v107, v101, v5
	v_add_u32_e32 v108, v101, v6
	v_add_u32_e32 v109, v101, v7
	v_add_u32_e32 v110, v101, v8
	v_add_u32_e32 v111, v15, v88
	v_add_u32_e32 v112, v13, v2
	v_add_u32_e32 v113, v11, v2
	v_readlane_b32 s5, v255, 11
	s_mov_b32 s16, s6
	v_readlane_b32 s7, v254, 57
	v_add_u32_e32 v226, v102, v93
	v_add_u32_e32 v227, v102, v94
	v_add_u32_e32 v228, v102, v95
	v_add_u32_e32 v229, v102, v96
	v_add_u32_e32 v230, v102, v97
	v_add_u32_e32 v231, v102, v98
	v_add_u32_e32 v232, v102, v99
	v_add_u32_e32 v233, v102, v100
	v_add_u32_e32 v234, v103, v93
	v_add_u32_e32 v235, v103, v94
	v_add_u32_e32 v236, v103, v95
	v_add_u32_e32 v237, v103, v96
	v_add_u32_e32 v238, v103, v97
	v_add_u32_e32 v239, v103, v98
	v_add_u32_e32 v240, v103, v99
	v_add_u32_e32 v241, v103, v100
	s_mov_b32 s99, 0
	s_branch .LBB0_804
.Lsp_drain:
	s_waitcnt lgkmcnt(0)
	v_lshrrev_b32_e32 v152, 3, v90
	v_and_b32_e32 v152, -4, v152
	v_mov_b32_e32 v153, 0
	v_lshlrev_b64 v[148:149], 9, v[152:153]
	v_lshl_or_b32 v148, v130, 1, v148
	v_lshl_add_u64 v[152:153], s[4:5], 0, v[148:149]
	v_mul_f32_e32 v0, v0, v132
	v_cvt_pk_bf16_f32 v0, v0, s0
	global_store_short v[152:153], v0, off
	v_mul_f32_e32 v0, v1, v133
	v_cvt_pk_bf16_f32 v0, v0, s0
	global_store_short v[152:153], v0, off offset:512
	v_mul_f32_e32 v0, v2, v134
	v_cvt_pk_bf16_f32 v0, v0, s0
	global_store_short v[152:153], v0, off offset:1024
	v_mul_f32_e32 v0, v3, v135
	v_cvt_pk_bf16_f32 v0, v0, s0
	global_store_short v[152:153], v0, off offset:1536
	v_mul_f32_e32 v0, v4, v136
	v_cvt_pk_bf16_f32 v4, v0, s0
	v_add_co_u32_e32 v0, vcc, s78, v152
	s_nop 0
	s_nop 0
	v_addc_co_u32_e32 v1, vcc, 0, v153, vcc
	v_add_co_u32_e32 v2, vcc, s93, v152
	v_readlane_b32 s8, v255, 17
	s_nop 0
	v_addc_co_u32_e32 v3, vcc, 0, v153, vcc
	global_store_short v[2:3], v4, off offset:-4096
	v_mul_f32_e32 v4, v5, v137
	v_cvt_pk_bf16_f32 v4, v4, s0
	global_store_short v[0:1], v4, off offset:512
	v_mul_f32_e32 v4, v6, v138
	v_cvt_pk_bf16_f32 v4, v4, s0
	global_store_short v[0:1], v4, off offset:1024
	v_mul_f32_e32 v4, v7, v139
	v_cvt_pk_bf16_f32 v4, v4, s0
	global_store_short v[0:1], v4, off offset:1536
	v_mul_f32_e32 v0, v8, v140
	v_cvt_pk_bf16_f32 v0, v0, s0
	global_store_short v[2:3], v0, off
	v_mul_f32_e32 v0, v9, v141
	v_cvt_pk_bf16_f32 v0, v0, s0
	global_store_short v[2:3], v0, off offset:512
	v_mul_f32_e32 v0, v10, v142
	v_cvt_pk_bf16_f32 v0, v0, s0
	global_store_short v[2:3], v0, off offset:1024
	v_mul_f32_e32 v0, v11, v143
	v_cvt_pk_bf16_f32 v0, v0, s0
	global_store_short v[2:3], v0, off offset:1536
	v_mul_f32_e32 v0, v12, v144
	v_cvt_pk_bf16_f32 v2, v0, s0
	v_add_co_u32_e32 v0, vcc, s3, v152
	v_readlane_b32 s9, v255, 18
	s_nop 0
	v_addc_co_u32_e32 v1, vcc, 0, v153, vcc
	global_store_short v[0:1], v2, off
	v_mul_f32_e32 v2, v13, v145
	v_cvt_pk_bf16_f32 v2, v2, s0
	global_store_short v[0:1], v2, off offset:512
	v_mul_f32_e32 v2, v14, v146
	v_cvt_pk_bf16_f32 v2, v2, s0
	global_store_short v[0:1], v2, off offset:1024
	v_mul_f32_e32 v2, v15, v147
	s_add_u32 s4, s4, s8
	v_cvt_pk_bf16_f32 v2, v2, s0
	s_addc_u32 s5, s5, s9
	global_store_short v[0:1], v2, off offset:1536
	s_branch .LBB0_810
.LBB0_803:
	s_or_b64 exec, exec, s[8:9]
	v_readlane_b32 s8, v253, 22
	s_add_i32 s14, s14, 1
	s_mov_b32 s99, 1
	s_nop 0
	v_lshl_add_u32 v152, v88, 2, s8
	ds_read_b128 v[132:135], v152
	ds_read_b128 v[136:139], v152 offset:32
	ds_read_b128 v[140:143], v152 offset:64
	ds_read_b128 v[144:147], v152 offset:96
	s_andn2_b64 vcc, exec, s[6:7]
	s_mov_b32 s16, s15
	s_nop 0
	s_cbranch_vccz .Lsp_drain
.LBB0_804:
	v_mov_b32_e32 v89, v90
	s_add_i32 s15, s16, s28
	s_and_b32 s17, s14, 1
	s_waitcnt lgkmcnt(0)
	s_barrier
	v_add_u32_e32 v150, v101, v92
	s_cmpk_gt_i32 s15, 0x7fff
	v_lshlrev_b32_e32 v88, 4, v89
	s_waitcnt vmcnt(33)
	ds_write_b128 v150, v[16:19]
	s_waitcnt vmcnt(32)
	ds_write_b128 v104, v[20:23] offset:512
	s_waitcnt vmcnt(31)
	ds_write_b128 v105, v[24:27] offset:1024
	s_waitcnt vmcnt(30)
	ds_write_b128 v106, v[28:31] offset:1536
	s_waitcnt vmcnt(29)
	ds_write_b128 v107, v[32:35] offset:2048
	s_waitcnt vmcnt(28)
	ds_write_b128 v108, v[36:39] offset:2560
	s_waitcnt vmcnt(27)
	ds_write_b128 v109, v[40:43] offset:3072
	s_waitcnt vmcnt(26)
	ds_write_b128 v110, v[44:47] offset:3584
	s_waitcnt vmcnt(25)
	ds_write_b128 v150, v[48:51] offset:4096
	s_waitcnt vmcnt(24)
	ds_write_b128 v104, v[52:55] offset:4608
	s_waitcnt vmcnt(23)
	ds_write_b128 v105, v[56:59] offset:5120
	s_waitcnt vmcnt(22)
	ds_write_b128 v106, v[60:63] offset:5632
	s_waitcnt vmcnt(21)
	ds_write_b128 v107, v[64:67] offset:6144
	s_waitcnt vmcnt(20)
	ds_write_b128 v108, v[68:71] offset:6656
	s_waitcnt vmcnt(19)
	ds_write_b128 v109, v[72:75] offset:7168
	s_waitcnt vmcnt(18)
	ds_write_b128 v110, v[76:79] offset:7680
	s_waitcnt vmcnt(0)
	ds_write_b128 v111, v[84:87]
	ds_write_b128 v111, v[80:83] offset:128
	s_cselect_b64 s[6:7], -1, 0
	s_cmp_eq_u32 s99, 0
	s_cbranch_scc1 .Lsp_noout
	v_lshrrev_b32_e32 v152, 3, v90
	v_and_b32_e32 v152, -4, v152
	v_mov_b32_e32 v153, 0
	v_lshlrev_b64 v[148:149], 9, v[152:153]
	v_lshl_or_b32 v148, v130, 1, v148
	v_lshl_add_u64 v[152:153], s[4:5], 0, v[148:149]
	v_mul_f32_e32 v0, v0, v132
	v_cvt_pk_bf16_f32 v0, v0, s0
	global_store_short v[152:153], v0, off
	v_mul_f32_e32 v0, v1, v133
	v_cvt_pk_bf16_f32 v0, v0, s0
	global_store_short v[152:153], v0, off offset:512
	v_mul_f32_e32 v0, v2, v134
	v_cvt_pk_bf16_f32 v0, v0, s0
	global_store_short v[152:153], v0, off offset:1024
	v_mul_f32_e32 v0, v3, v135
	v_cvt_pk_bf16_f32 v0, v0, s0
	global_store_short v[152:153], v0, off offset:1536
	v_mul_f32_e32 v0, v4, v136
	v_cvt_pk_bf16_f32 v4, v0, s0
	v_add_co_u32_e32 v0, vcc, s78, v152
	s_nop 0
	s_nop 0
	v_addc_co_u32_e32 v1, vcc, 0, v153, vcc
	v_add_co_u32_e32 v2, vcc, s93, v152
	v_readlane_b32 s8, v255, 17
	s_nop 0
	v_addc_co_u32_e32 v3, vcc, 0, v153, vcc
	global_store_short v[2:3], v4, off offset:-4096
	v_mul_f32_e32 v4, v5, v137
	v_cvt_pk_bf16_f32 v4, v4, s0
	global_store_short v[0:1], v4, off offset:512
	v_mul_f32_e32 v4, v6, v138
	v_cvt_pk_bf16_f32 v4, v4, s0
	global_store_short v[0:1], v4, off offset:1024
	v_mul_f32_e32 v4, v7, v139
	v_cvt_pk_bf16_f32 v4, v4, s0
	global_store_short v[0:1], v4, off offset:1536
	v_mul_f32_e32 v0, v8, v140
	v_cvt_pk_bf16_f32 v0, v0, s0
	global_store_short v[2:3], v0, off
	v_mul_f32_e32 v0, v9, v141
	v_cvt_pk_bf16_f32 v0, v0, s0
	global_store_short v[2:3], v0, off offset:512
	v_mul_f32_e32 v0, v10, v142
	v_cvt_pk_bf16_f32 v0, v0, s0
	global_store_short v[2:3], v0, off offset:1024
	v_mul_f32_e32 v0, v11, v143
	v_cvt_pk_bf16_f32 v0, v0, s0
	global_store_short v[2:3], v0, off offset:1536
	v_mul_f32_e32 v0, v12, v144
	v_cvt_pk_bf16_f32 v2, v0, s0
	v_add_co_u32_e32 v0, vcc, s3, v152
	v_readlane_b32 s9, v255, 18
	s_nop 0
	v_addc_co_u32_e32 v1, vcc, 0, v153, vcc
	global_store_short v[0:1], v2, off
	v_mul_f32_e32 v2, v13, v145
	v_cvt_pk_bf16_f32 v2, v2, s0
	global_store_short v[0:1], v2, off offset:512
	v_mul_f32_e32 v2, v14, v146
	v_cvt_pk_bf16_f32 v2, v2, s0
	global_store_short v[0:1], v2, off offset:1024
	v_mul_f32_e32 v2, v15, v147
	s_add_u32 s4, s4, s8
	v_cvt_pk_bf16_f32 v2, v2, s0
	s_addc_u32 s5, s5, s9
	global_store_short v[0:1], v2, off offset:1536
.Lsp_noout:
	s_cmp_lt_i32 s15, 0x8000
	v_add_u32_e32 v151, 0, v88
	s_waitcnt lgkmcnt(0)
	s_barrier
	s_cselect_b32 s8, s15, s16
	v_add_u32_e32 v77, 0x20000, v151
	s_ashr_i32 s9, s8, 31
	ds_read_b128 v[0:3], v226
	ds_read_b128 v[4:7], v77
	s_lshr_b32 s10, s9, 20
	s_add_i32 s10, s8, s10
	s_ashr_i32 s10, s10, 12
	s_ashr_i32 s11, s10, 31
	s_lshl_b64 s[12:13], s[10:11], 21
	v_readlane_b32 s11, v253, 2
	v_and_b32_e32 v130, 31, v89
	s_waitcnt lgkmcnt(0)
	v_mfma_f32_32x32x16_bf16 v[0:15], v[0:3], v[4:7], 0
	s_add_u32 s12, s11, s12
	v_readlane_b32 s11, v253, 3
	v_lshlrev_b32_e32 v76, 4, v130
	s_addc_u32 s13, s11, s13
	v_lshl_or_b32 v16, v121, 9, v76
	global_load_dwordx4 v[16:19], v16, s[12:13]
	ds_read_b128 v[20:23], v227
	ds_read_b128 v[24:27], v77 offset:1024
	s_waitcnt lgkmcnt(0)
	v_mfma_f32_32x32x16_bf16 v[0:15], v[20:23], v[24:27], v[0:15]
	v_lshl_or_b32 v20, v123, 9, v76
	global_load_dwordx4 v[20:23], v20, s[12:13]
	ds_read_b128 v[24:27], v228
	ds_read_b128 v[28:31], v77 offset:2048
	v_add_u32_e32 v80, s44, v89
	s_movk_i32 s11, 0x100
	s_waitcnt lgkmcnt(0)
	v_mfma_f32_32x32x16_bf16 v[0:15], v[24:27], v[28:31], v[0:15]
	v_lshl_or_b32 v24, v116, 9, v76
	global_load_dwordx4 v[24:27], v24, s[12:13]
	ds_read_b128 v[28:31], v229
	ds_read_b128 v[32:35], v77 offset:3072
	v_cmp_gt_i32_e32 vcc, s11, v80
	s_waitcnt lgkmcnt(0)
	v_mfma_f32_32x32x16_bf16 v[0:15], v[28:31], v[32:35], v[0:15]
	v_lshl_or_b32 v28, v124, 9, v76
	global_load_dwordx4 v[28:31], v28, s[12:13]
	ds_read_b128 v[32:35], v230
	ds_read_b128 v[36:39], v77 offset:4096
	s_waitcnt lgkmcnt(0)
	v_mfma_f32_32x32x16_bf16 v[0:15], v[32:35], v[36:39], v[0:15]
	v_lshl_or_b32 v32, v119, 9, v76
	global_load_dwordx4 v[32:35], v32, s[12:13]
	ds_read_b128 v[36:39], v231
	ds_read_b128 v[40:43], v77 offset:5120
	s_waitcnt lgkmcnt(0)
	v_mfma_f32_32x32x16_bf16 v[0:15], v[36:39], v[40:43], v[0:15]
	v_lshl_or_b32 v36, v120, 9, v76
	global_load_dwordx4 v[36:39], v36, s[12:13]
	ds_read_b128 v[40:43], v232
	ds_read_b128 v[44:47], v77 offset:6144
	s_waitcnt lgkmcnt(0)
	v_mfma_f32_32x32x16_bf16 v[0:15], v[40:43], v[44:47], v[0:15]
	v_lshl_or_b32 v40, v117, 9, v76
	global_load_dwordx4 v[40:43], v40, s[12:13]
	ds_read_b128 v[44:47], v233
	ds_read_b128 v[48:51], v77 offset:7168
	s_waitcnt lgkmcnt(0)
	v_mfma_f32_32x32x16_bf16 v[0:15], v[44:47], v[48:51], v[0:15]
	v_lshl_or_b32 v44, v125, 9, v76
	global_load_dwordx4 v[44:47], v44, s[12:13]
	ds_read_b128 v[48:51], v234
	ds_read_b128 v[52:55], v77 offset:8192
	s_waitcnt lgkmcnt(0)
	v_mfma_f32_32x32x16_bf16 v[0:15], v[48:51], v[52:55], v[0:15]
	v_lshl_or_b32 v48, v118, 9, v76
	global_load_dwordx4 v[48:51], v48, s[12:13]
	ds_read_b128 v[52:55], v235
	ds_read_b128 v[56:59], v77 offset:9216
	s_waitcnt lgkmcnt(0)
	v_mfma_f32_32x32x16_bf16 v[0:15], v[52:55], v[56:59], v[0:15]
	v_lshl_or_b32 v52, v114, 9, v76
	global_load_dwordx4 v[52:55], v52, s[12:13]
	ds_read_b128 v[56:59], v236
	ds_read_b128 v[60:63], v77 offset:10240
	s_waitcnt lgkmcnt(0)
	v_mfma_f32_32x32x16_bf16 v[0:15], v[56:59], v[60:63], v[0:15]
	v_lshl_or_b32 v56, v115, 9, v76
	global_load_dwordx4 v[56:59], v56, s[12:13]
	ds_read_b128 v[60:63], v237
	ds_read_b128 v[64:67], v77 offset:11264
	s_waitcnt lgkmcnt(0)
	v_mfma_f32_32x32x16_bf16 v[0:15], v[60:63], v[64:67], v[0:15]
	v_lshl_or_b32 v60, v122, 9, v76
	global_load_dwordx4 v[60:63], v60, s[12:13]
	ds_read_b128 v[64:67], v238
	ds_read_b128 v[68:71], v77 offset:12288
	s_waitcnt lgkmcnt(0)
	v_mfma_f32_32x32x16_bf16 v[0:15], v[64:67], v[68:71], v[0:15]
	v_lshl_or_b32 v64, v126, 9, v76
	global_load_dwordx4 v[64:67], v64, s[12:13]
	ds_read_b128 v[68:71], v239
	ds_read_b128 v[72:75], v77 offset:13312
	s_waitcnt lgkmcnt(0)
	v_mfma_f32_32x32x16_bf16 v[0:15], v[68:71], v[72:75], v[0:15]
	v_lshl_or_b32 v68, v127, 9, v76
	global_load_dwordx4 v[68:71], v68, s[12:13]
	ds_read_b128 v[72:75], v240
	ds_read_b128 v[82:85], v77 offset:14336
	s_waitcnt lgkmcnt(0)
	v_mfma_f32_32x32x16_bf16 v[0:15], v[72:75], v[82:85], v[0:15]
	v_lshl_or_b32 v72, v128, 9, v76
	v_lshl_or_b32 v76, v129, 9, v76
	global_load_dwordx4 v[72:75], v72, s[12:13]
	ds_read_b128 v[82:85], v241
	ds_read_b128 v[114:117], v77 offset:15360
	global_load_dwordx4 v[76:79], v76, s[12:13]
	s_waitcnt lgkmcnt(0)
	v_mfma_f32_32x32x16_bf16 v[0:15], v[82:85], v[114:117], v[0:15]
	s_and_saveexec_b64 s[12:13], vcc
	s_cbranch_execz .LBB0_808
	s_lshl_b32 s10, s10, 12
	s_sub_i32 s18, s8, s10
	v_cmp_ge_i32_e32 vcc, s18, v80
	v_mov_b32_e32 v81, 0x1000
	s_and_saveexec_b64 s[10:11], vcc
	s_cbranch_execz .LBB0_807
	v_sub_u32_e32 v81, s18, v91
	v_mov_b32_e32 v82, 0x7f
	v_med3_i32 v81, v81, 0, v82
	v_add_u32_e32 v81, 0, v81
	v_add_u32_e32 v81, 0x25e80, v81
	ds_read_u8 v81, v81
	s_waitcnt lgkmcnt(0)
	v_lshlrev_b32_e32 v81, 7, v81
